# hand-written gates epilogue (16 independent sigmoid chains per store) replacing gfold; rest as v44
# baseline (speedup 1.0000x reference)
; __device__ __forceinline__ float fsigmoid(float x) { return __builtin_amdgcn_rcpf(1.0f + __builtin_amdgcn_exp2f(-1.44269504f * x)); }
; __device__ __forceinline__ unsigned pk4_u8(float a, float b, float c, float d) {
;     const unsigned ya = __builtin_bit_cast(unsigned, a * 255.0f + 8388608.0f), yb = __builtin_bit_cast(unsigned, b * 255.0f + 8388608.0f), yc = __builtin_bit_cast(unsigned, c * 255.0f + 8388608.0f), yd = __builtin_bit_cast(unsigned, d * 255.0f + 8388608.0f);
;     const unsigned w01 = __builtin_amdgcn_perm(yb, ya, 0x0c0c0400u), w23 = __builtin_amdgcn_perm(yd, yc, 0x0c0c0400u);
;     return __builtin_amdgcn_perm(w23, w01, 0x05040100u); }
;     __device__ __forceinline__ void operator()(AccRef acc, const GUnit& u, int wr, int wc, int fr, int fq) const {
;         const int pm = u.x0, pn = u.x1; unsigned char* base = (pn < 8 ? GZF : GZS) + (size_t)(pm * 256 + wr * 64 + fr) * D + (pn & 7) * 256 + wc * 64 + 16 * fq;
; #pragma unroll
;         for (int ai = 0; ai < 2; ++ai)
; #pragma unroll
;             for (int m = 0; m < 4; ++m) { u32x4 w;
; #pragma unroll
;                 for (int bj = 0; bj < 2; ++bj)
; #pragma unroll
;                     for (int n = 0; n < 2; ++n) { const f32x4 v = acc[ai][bj][m][n]; w[bj * 2 + n] = pk4_u8(fsigmoid(v[0] * W8_INV), fsigmoid(v[1] * W8_INV), fsigmoid(v[2] * W8_INV), fsigmoid(v[3] * W8_INV)); }
;                 *(u32x4*)(base + (size_t)(ai * 128 + m * 16) * D) = w; }
.LBB0_431:
	s_nop 15
	s_nop 7
	v_lshl_add_u32 v2, s8, 8, v190
	s_cmp_lt_i32 s73, 8
	v_ashrrev_i32_e32 v3, 31, v2
	s_cselect_b32 s25, s41, s59
	s_cselect_b32 s24, s40, s53
	v_lshlrev_b64 v[2:3], 11, v[2:3]
	s_lshl_b32 s8, s73, 8
	v_lshl_add_u64 v[2:3], s[24:25], 0, v[2:3]
	s_and_b32 s8, s8, 0x700
	v_lshl_add_u64 v[2:3], v[2:3], 0, s[8:9]
	v_lshl_add_u64 v[2:3], v[2:3], 0, s[14:15]
	v_lshl_add_u64 v[2:3], v[2:3], 0, v[162:163]
	v_mul_f32_e32 v236, 0xbcb8aa3b, v158
	v_mul_f32_e32 v237, 0xbcb8aa3b, v159
	v_mul_f32_e32 v238, 0xbcb8aa3b, v160
	v_mul_f32_e32 v239, 0xbcb8aa3b, v161
	v_mul_f32_e32 v240, 0xbcb8aa3b, v154
	v_mul_f32_e32 v241, 0xbcb8aa3b, v155
	v_mul_f32_e32 v242, 0xbcb8aa3b, v156
	v_mul_f32_e32 v243, 0xbcb8aa3b, v157
	v_mul_f32_e32 v244, 0xbcb8aa3b, v150
	v_mul_f32_e32 v245, 0xbcb8aa3b, v151
	v_mul_f32_e32 v246, 0xbcb8aa3b, v152
	v_mul_f32_e32 v247, 0xbcb8aa3b, v153
	v_mul_f32_e32 v248, 0xbcb8aa3b, v146
	v_mul_f32_e32 v249, 0xbcb8aa3b, v147
	v_mul_f32_e32 v250, 0xbcb8aa3b, v148
	v_mul_f32_e32 v251, 0xbcb8aa3b, v149
	v_exp_f32_e32 v236, v236
	v_exp_f32_e32 v237, v237
	v_exp_f32_e32 v238, v238
	v_exp_f32_e32 v239, v239
	v_exp_f32_e32 v240, v240
	v_exp_f32_e32 v241, v241
	v_exp_f32_e32 v242, v242
	v_exp_f32_e32 v243, v243
	v_exp_f32_e32 v244, v244
	v_exp_f32_e32 v245, v245
	v_exp_f32_e32 v246, v246
	v_exp_f32_e32 v247, v247
	v_exp_f32_e32 v248, v248
	v_exp_f32_e32 v249, v249
	v_exp_f32_e32 v250, v250
	v_exp_f32_e32 v251, v251
	v_add_f32_e32 v236, 1.0, v236
	v_add_f32_e32 v237, 1.0, v237
	v_add_f32_e32 v238, 1.0, v238
	v_add_f32_e32 v239, 1.0, v239
	v_add_f32_e32 v240, 1.0, v240
	v_add_f32_e32 v241, 1.0, v241
	v_add_f32_e32 v242, 1.0, v242
	v_add_f32_e32 v243, 1.0, v243
	v_add_f32_e32 v244, 1.0, v244
	v_add_f32_e32 v245, 1.0, v245
	v_add_f32_e32 v246, 1.0, v246
	v_add_f32_e32 v247, 1.0, v247
	v_add_f32_e32 v248, 1.0, v248
	v_add_f32_e32 v249, 1.0, v249
	v_add_f32_e32 v250, 1.0, v250
	v_add_f32_e32 v251, 1.0, v251
	v_rcp_f32_e32 v236, v236
	v_rcp_f32_e32 v237, v237
	v_rcp_f32_e32 v238, v238
	v_rcp_f32_e32 v239, v239
	v_rcp_f32_e32 v240, v240
	v_rcp_f32_e32 v241, v241
	v_rcp_f32_e32 v242, v242
	v_rcp_f32_e32 v243, v243
	v_rcp_f32_e32 v244, v244
	v_rcp_f32_e32 v245, v245
	v_rcp_f32_e32 v246, v246
	v_rcp_f32_e32 v247, v247
	v_rcp_f32_e32 v248, v248
	v_rcp_f32_e32 v249, v249
	v_rcp_f32_e32 v250, v250
	v_rcp_f32_e32 v251, v251
	v_fmamk_f32 v236, v236, 0x437f0000, v196
	v_fmamk_f32 v237, v237, 0x437f0000, v196
	v_fmamk_f32 v238, v238, 0x437f0000, v196
	v_fmamk_f32 v239, v239, 0x437f0000, v196
	v_fmamk_f32 v240, v240, 0x437f0000, v196
	v_fmamk_f32 v241, v241, 0x437f0000, v196
	v_fmamk_f32 v242, v242, 0x437f0000, v196
	v_fmamk_f32 v243, v243, 0x437f0000, v196
	v_fmamk_f32 v244, v244, 0x437f0000, v196
	v_fmamk_f32 v245, v245, 0x437f0000, v196
	v_fmamk_f32 v246, v246, 0x437f0000, v196
	v_fmamk_f32 v247, v247, 0x437f0000, v196
	v_fmamk_f32 v248, v248, 0x437f0000, v196
	v_fmamk_f32 v249, v249, 0x437f0000, v196
	v_fmamk_f32 v250, v250, 0x437f0000, v196
	v_fmamk_f32 v251, v251, 0x437f0000, v196
	v_perm_b32 v236, v237, v236, s67
	v_perm_b32 v238, v239, v238, s67
	v_perm_b32 v240, v241, v240, s67
	v_perm_b32 v242, v243, v242, s67
	v_perm_b32 v244, v245, v244, s67
	v_perm_b32 v246, v247, v246, s67
	v_perm_b32 v248, v249, v248, s67
	v_perm_b32 v250, v251, v250, s67
	v_perm_b32 v4, v238, v236, s68
	v_perm_b32 v5, v242, v240, s68
	v_perm_b32 v6, v246, v244, s68
	v_perm_b32 v7, v250, v248, s68
	global_store_dwordx4 v[2:3], v[4:7], off
	v_mul_f32_e32 v236, 0xbcb8aa3b, v142
	v_mul_f32_e32 v237, 0xbcb8aa3b, v143
	v_mul_f32_e32 v238, 0xbcb8aa3b, v144
	v_mul_f32_e32 v239, 0xbcb8aa3b, v145
	v_mul_f32_e32 v240, 0xbcb8aa3b, v138
	v_mul_f32_e32 v241, 0xbcb8aa3b, v139
	v_mul_f32_e32 v242, 0xbcb8aa3b, v140
	v_mul_f32_e32 v243, 0xbcb8aa3b, v141
	v_mul_f32_e32 v244, 0xbcb8aa3b, v134
	v_mul_f32_e32 v245, 0xbcb8aa3b, v135
	v_mul_f32_e32 v246, 0xbcb8aa3b, v136
	v_mul_f32_e32 v247, 0xbcb8aa3b, v137
	v_mul_f32_e32 v248, 0xbcb8aa3b, v130
	v_mul_f32_e32 v249, 0xbcb8aa3b, v131
	v_mul_f32_e32 v250, 0xbcb8aa3b, v132
	v_mul_f32_e32 v251, 0xbcb8aa3b, v133
	v_exp_f32_e32 v236, v236
	v_exp_f32_e32 v237, v237
	v_exp_f32_e32 v238, v238
	v_exp_f32_e32 v239, v239
	v_exp_f32_e32 v240, v240
	v_exp_f32_e32 v241, v241
	v_exp_f32_e32 v242, v242
	v_exp_f32_e32 v243, v243
	v_exp_f32_e32 v244, v244
	v_exp_f32_e32 v245, v245
	v_exp_f32_e32 v246, v246
	v_exp_f32_e32 v247, v247
	v_exp_f32_e32 v248, v248
	v_exp_f32_e32 v249, v249
	v_exp_f32_e32 v250, v250
	v_exp_f32_e32 v251, v251
	v_add_f32_e32 v236, 1.0, v236
	v_add_f32_e32 v237, 1.0, v237
	v_add_f32_e32 v238, 1.0, v238
	v_add_f32_e32 v239, 1.0, v239
	v_add_f32_e32 v240, 1.0, v240
	v_add_f32_e32 v241, 1.0, v241
	v_add_f32_e32 v242, 1.0, v242
	v_add_f32_e32 v243, 1.0, v243
	v_add_f32_e32 v244, 1.0, v244
	v_add_f32_e32 v245, 1.0, v245
	v_add_f32_e32 v246, 1.0, v246
	v_add_f32_e32 v247, 1.0, v247
	v_add_f32_e32 v248, 1.0, v248
	v_add_f32_e32 v249, 1.0, v249
	v_add_f32_e32 v250, 1.0, v250
	v_add_f32_e32 v251, 1.0, v251
	v_rcp_f32_e32 v236, v236
	v_rcp_f32_e32 v237, v237
	v_rcp_f32_e32 v238, v238
	v_rcp_f32_e32 v239, v239
	v_rcp_f32_e32 v240, v240
	v_rcp_f32_e32 v241, v241
	v_rcp_f32_e32 v242, v242
	v_rcp_f32_e32 v243, v243
	v_rcp_f32_e32 v244, v244
	v_rcp_f32_e32 v245, v245
	v_rcp_f32_e32 v246, v246
	v_rcp_f32_e32 v247, v247
	v_rcp_f32_e32 v248, v248
	v_rcp_f32_e32 v249, v249
	v_rcp_f32_e32 v250, v250
	v_rcp_f32_e32 v251, v251
	v_fmamk_f32 v236, v236, 0x437f0000, v196
	v_fmamk_f32 v237, v237, 0x437f0000, v196
	v_fmamk_f32 v238, v238, 0x437f0000, v196
	v_fmamk_f32 v239, v239, 0x437f0000, v196
	v_fmamk_f32 v240, v240, 0x437f0000, v196
; __device__ __forceinline__ float fsigmoid(float x) { return __builtin_amdgcn_rcpf(1.0f + __builtin_amdgcn_exp2f(-1.44269504f * x)); }
; __device__ __forceinline__ unsigned pk4_u8(float a, float b, float c, float d) {
;     const unsigned ya = __builtin_bit_cast(unsigned, a * 255.0f + 8388608.0f), yb = __builtin_bit_cast(unsigned, b * 255.0f + 8388608.0f), yc = __builtin_bit_cast(unsigned, c * 255.0f + 8388608.0f), yd = __builtin_bit_cast(unsigned, d * 255.0f + 8388608.0f);
;     const unsigned w01 = __builtin_amdgcn_perm(yb, ya, 0x0c0c0400u), w23 = __builtin_amdgcn_perm(yd, yc, 0x0c0c0400u);
;     return __builtin_amdgcn_perm(w23, w01, 0x05040100u); }
;     __device__ __forceinline__ void operator()(AccRef acc, const GUnit& u, int wr, int wc, int fr, int fq) const {
;         const int pm = u.x0, pn = u.x1; unsigned char* base = (pn < 8 ? GZF : GZS) + (size_t)(pm * 256 + wr * 64 + fr) * D + (pn & 7) * 256 + wc * 64 + 16 * fq;
; #pragma unroll
;         for (int ai = 0; ai < 2; ++ai)
; #pragma unroll
;             for (int m = 0; m < 4; ++m) { u32x4 w;
; #pragma unroll
;                 for (int bj = 0; bj < 2; ++bj)
; #pragma unroll
;                     for (int n = 0; n < 2; ++n) { const f32x4 v = acc[ai][bj][m][n]; w[bj * 2 + n] = pk4_u8(fsigmoid(v[0] * W8_INV), fsigmoid(v[1] * W8_INV), fsigmoid(v[2] * W8_INV), fsigmoid(v[3] * W8_INV)); }
;                 *(u32x4*)(base + (size_t)(ai * 128 + m * 16) * D) = w; }
	v_fmamk_f32 v241, v241, 0x437f0000, v196
	v_fmamk_f32 v242, v242, 0x437f0000, v196
	v_fmamk_f32 v243, v243, 0x437f0000, v196
	v_fmamk_f32 v244, v244, 0x437f0000, v196
	v_fmamk_f32 v245, v245, 0x437f0000, v196
	v_fmamk_f32 v246, v246, 0x437f0000, v196
	v_fmamk_f32 v247, v247, 0x437f0000, v196
	v_fmamk_f32 v248, v248, 0x437f0000, v196
	v_fmamk_f32 v249, v249, 0x437f0000, v196
	v_fmamk_f32 v250, v250, 0x437f0000, v196
	v_fmamk_f32 v251, v251, 0x437f0000, v196
	v_perm_b32 v236, v237, v236, s67
	v_perm_b32 v238, v239, v238, s67
	v_perm_b32 v240, v241, v240, s67
	v_perm_b32 v242, v243, v242, s67
	v_perm_b32 v244, v245, v244, s67
	v_perm_b32 v246, v247, v246, s67
	v_perm_b32 v248, v249, v248, s67
	v_perm_b32 v250, v251, v250, s67
	v_perm_b32 v4, v238, v236, s68
	v_perm_b32 v5, v242, v240, s68
	v_perm_b32 v6, v246, v244, s68
	v_perm_b32 v7, v250, v248, s68
	v_add_co_u32_e32 v8, vcc, s63, v2
	s_nop 1
	v_addc_co_u32_e32 v9, vcc, 0, v3, vcc
	global_store_dwordx4 v[8:9], v[4:7], off
	v_mul_f32_e32 v236, 0xbcb8aa3b, v126
	v_mul_f32_e32 v237, 0xbcb8aa3b, v127
	v_mul_f32_e32 v238, 0xbcb8aa3b, v128
	v_mul_f32_e32 v239, 0xbcb8aa3b, v129
	v_mul_f32_e32 v240, 0xbcb8aa3b, v122
	v_mul_f32_e32 v241, 0xbcb8aa3b, v123
	v_mul_f32_e32 v242, 0xbcb8aa3b, v124
	v_mul_f32_e32 v243, 0xbcb8aa3b, v125
	v_mul_f32_e32 v244, 0xbcb8aa3b, v118
	v_mul_f32_e32 v245, 0xbcb8aa3b, v119
	v_mul_f32_e32 v246, 0xbcb8aa3b, v120
	v_mul_f32_e32 v247, 0xbcb8aa3b, v121
	v_mul_f32_e32 v248, 0xbcb8aa3b, v114
	v_mul_f32_e32 v249, 0xbcb8aa3b, v115
	v_mul_f32_e32 v250, 0xbcb8aa3b, v116
	v_mul_f32_e32 v251, 0xbcb8aa3b, v117
	v_exp_f32_e32 v236, v236
	v_exp_f32_e32 v237, v237
	v_exp_f32_e32 v238, v238
	v_exp_f32_e32 v239, v239
	v_exp_f32_e32 v240, v240
	v_exp_f32_e32 v241, v241
	v_exp_f32_e32 v242, v242
	v_exp_f32_e32 v243, v243
	v_exp_f32_e32 v244, v244
	v_exp_f32_e32 v245, v245
	v_exp_f32_e32 v246, v246
	v_exp_f32_e32 v247, v247
	v_exp_f32_e32 v248, v248
	v_exp_f32_e32 v249, v249
	v_exp_f32_e32 v250, v250
	v_exp_f32_e32 v251, v251
	v_add_f32_e32 v236, 1.0, v236
	v_add_f32_e32 v237, 1.0, v237
	v_add_f32_e32 v238, 1.0, v238
	v_add_f32_e32 v239, 1.0, v239
	v_add_f32_e32 v240, 1.0, v240
	v_add_f32_e32 v241, 1.0, v241
	v_add_f32_e32 v242, 1.0, v242
	v_add_f32_e32 v243, 1.0, v243
	v_add_f32_e32 v244, 1.0, v244
	v_add_f32_e32 v245, 1.0, v245
	v_add_f32_e32 v246, 1.0, v246
	v_add_f32_e32 v247, 1.0, v247
	v_add_f32_e32 v248, 1.0, v248
	v_add_f32_e32 v249, 1.0, v249
	v_add_f32_e32 v250, 1.0, v250
	v_add_f32_e32 v251, 1.0, v251
	v_rcp_f32_e32 v236, v236
	v_rcp_f32_e32 v237, v237
	v_rcp_f32_e32 v238, v238
	v_rcp_f32_e32 v239, v239
	v_rcp_f32_e32 v240, v240
	v_rcp_f32_e32 v241, v241
	v_rcp_f32_e32 v242, v242
	v_rcp_f32_e32 v243, v243
	v_rcp_f32_e32 v244, v244
	v_rcp_f32_e32 v245, v245
	v_rcp_f32_e32 v246, v246
	v_rcp_f32_e32 v247, v247
	v_rcp_f32_e32 v248, v248
	v_rcp_f32_e32 v249, v249
	v_rcp_f32_e32 v250, v250
	v_rcp_f32_e32 v251, v251
	v_fmamk_f32 v236, v236, 0x437f0000, v196
	v_fmamk_f32 v237, v237, 0x437f0000, v196
	v_fmamk_f32 v238, v238, 0x437f0000, v196
	v_fmamk_f32 v239, v239, 0x437f0000, v196
	v_fmamk_f32 v240, v240, 0x437f0000, v196
	v_fmamk_f32 v241, v241, 0x437f0000, v196
	v_fmamk_f32 v242, v242, 0x437f0000, v196
	v_fmamk_f32 v243, v243, 0x437f0000, v196
	v_fmamk_f32 v244, v244, 0x437f0000, v196
	v_fmamk_f32 v245, v245, 0x437f0000, v196
	v_fmamk_f32 v246, v246, 0x437f0000, v196
	v_fmamk_f32 v247, v247, 0x437f0000, v196
	v_fmamk_f32 v248, v248, 0x437f0000, v196
	v_fmamk_f32 v249, v249, 0x437f0000, v196
	v_fmamk_f32 v250, v250, 0x437f0000, v196
	v_fmamk_f32 v251, v251, 0x437f0000, v196
	v_perm_b32 v236, v237, v236, s67
	v_perm_b32 v238, v239, v238, s67
	v_perm_b32 v240, v241, v240, s67
	v_perm_b32 v242, v243, v242, s67
	v_perm_b32 v244, v245, v244, s67
	v_perm_b32 v246, v247, v246, s67
	v_perm_b32 v248, v249, v248, s67
	v_perm_b32 v250, v251, v250, s67
	v_perm_b32 v4, v238, v236, s68
	v_perm_b32 v5, v242, v240, s68
	v_perm_b32 v6, v246, v244, s68
	v_perm_b32 v7, v250, v248, s68
	v_add_co_u32_e32 v8, vcc, s52, v2
	s_nop 1
	v_addc_co_u32_e32 v9, vcc, 0, v3, vcc
	global_store_dwordx4 v[8:9], v[4:7], off
	v_mul_f32_e32 v236, 0xbcb8aa3b, v110
	v_mul_f32_e32 v237, 0xbcb8aa3b, v111
	v_mul_f32_e32 v238, 0xbcb8aa3b, v112
	v_mul_f32_e32 v239, 0xbcb8aa3b, v113
	v_mul_f32_e32 v240, 0xbcb8aa3b, v106
	v_mul_f32_e32 v241, 0xbcb8aa3b, v107
	v_mul_f32_e32 v242, 0xbcb8aa3b, v108
	v_mul_f32_e32 v243, 0xbcb8aa3b, v109
	v_mul_f32_e32 v244, 0xbcb8aa3b, v102
	v_mul_f32_e32 v245, 0xbcb8aa3b, v103
	v_mul_f32_e32 v246, 0xbcb8aa3b, v104
	v_mul_f32_e32 v247, 0xbcb8aa3b, v105
	v_mul_f32_e32 v248, 0xbcb8aa3b, v98
	v_mul_f32_e32 v249, 0xbcb8aa3b, v99
	v_mul_f32_e32 v250, 0xbcb8aa3b, v100
	v_mul_f32_e32 v251, 0xbcb8aa3b, v101
	v_exp_f32_e32 v236, v236
	v_exp_f32_e32 v237, v237
	v_exp_f32_e32 v238, v238
	v_exp_f32_e32 v239, v239
	v_exp_f32_e32 v240, v240
	v_exp_f32_e32 v241, v241
	v_exp_f32_e32 v242, v242
	v_exp_f32_e32 v243, v243
	v_exp_f32_e32 v244, v244
	v_exp_f32_e32 v245, v245
	v_exp_f32_e32 v246, v246
	v_exp_f32_e32 v247, v247
	v_exp_f32_e32 v248, v248
	v_exp_f32_e32 v249, v249
	v_exp_f32_e32 v250, v250
	v_exp_f32_e32 v251, v251
	v_add_f32_e32 v236, 1.0, v236
	v_add_f32_e32 v237, 1.0, v237
	v_add_f32_e32 v238, 1.0, v238
	v_add_f32_e32 v239, 1.0, v239
	v_add_f32_e32 v240, 1.0, v240
	v_add_f32_e32 v241, 1.0, v241
	v_add_f32_e32 v242, 1.0, v242
	v_add_f32_e32 v243, 1.0, v243
	v_add_f32_e32 v244, 1.0, v244
	v_add_f32_e32 v245, 1.0, v245
	v_add_f32_e32 v246, 1.0, v246
	v_add_f32_e32 v247, 1.0, v247
	v_add_f32_e32 v248, 1.0, v248
	v_add_f32_e32 v249, 1.0, v249
	v_add_f32_e32 v250, 1.0, v250
	v_add_f32_e32 v251, 1.0, v251
; __device__ __forceinline__ float fsigmoid(float x) { return __builtin_amdgcn_rcpf(1.0f + __builtin_amdgcn_exp2f(-1.44269504f * x)); }
; __device__ __forceinline__ unsigned pk4_u8(float a, float b, float c, float d) {
;     const unsigned ya = __builtin_bit_cast(unsigned, a * 255.0f + 8388608.0f), yb = __builtin_bit_cast(unsigned, b * 255.0f + 8388608.0f), yc = __builtin_bit_cast(unsigned, c * 255.0f + 8388608.0f), yd = __builtin_bit_cast(unsigned, d * 255.0f + 8388608.0f);
;     const unsigned w01 = __builtin_amdgcn_perm(yb, ya, 0x0c0c0400u), w23 = __builtin_amdgcn_perm(yd, yc, 0x0c0c0400u);
;     return __builtin_amdgcn_perm(w23, w01, 0x05040100u); }
;     __device__ __forceinline__ void operator()(AccRef acc, const GUnit& u, int wr, int wc, int fr, int fq) const {
;         const int pm = u.x0, pn = u.x1; unsigned char* base = (pn < 8 ? GZF : GZS) + (size_t)(pm * 256 + wr * 64 + fr) * D + (pn & 7) * 256 + wc * 64 + 16 * fq;
; #pragma unroll
;         for (int ai = 0; ai < 2; ++ai)
; #pragma unroll
;             for (int m = 0; m < 4; ++m) { u32x4 w;
; #pragma unroll
;                 for (int bj = 0; bj < 2; ++bj)
; #pragma unroll
;                     for (int n = 0; n < 2; ++n) { const f32x4 v = acc[ai][bj][m][n]; w[bj * 2 + n] = pk4_u8(fsigmoid(v[0] * W8_INV), fsigmoid(v[1] * W8_INV), fsigmoid(v[2] * W8_INV), fsigmoid(v[3] * W8_INV)); }
;                 *(u32x4*)(base + (size_t)(ai * 128 + m * 16) * D) = w; }
	v_rcp_f32_e32 v236, v236
	v_rcp_f32_e32 v237, v237
	v_rcp_f32_e32 v238, v238
	v_rcp_f32_e32 v239, v239
	v_rcp_f32_e32 v240, v240
	v_rcp_f32_e32 v241, v241
	v_rcp_f32_e32 v242, v242
	v_rcp_f32_e32 v243, v243
	v_rcp_f32_e32 v244, v244
	v_rcp_f32_e32 v245, v245
	v_rcp_f32_e32 v246, v246
	v_rcp_f32_e32 v247, v247
	v_rcp_f32_e32 v248, v248
	v_rcp_f32_e32 v249, v249
	v_rcp_f32_e32 v250, v250
	v_rcp_f32_e32 v251, v251
	v_fmamk_f32 v236, v236, 0x437f0000, v196
	v_fmamk_f32 v237, v237, 0x437f0000, v196
	v_fmamk_f32 v238, v238, 0x437f0000, v196
	v_fmamk_f32 v239, v239, 0x437f0000, v196
	v_fmamk_f32 v240, v240, 0x437f0000, v196
	v_fmamk_f32 v241, v241, 0x437f0000, v196
	v_fmamk_f32 v242, v242, 0x437f0000, v196
	v_fmamk_f32 v243, v243, 0x437f0000, v196
	v_fmamk_f32 v244, v244, 0x437f0000, v196
	v_fmamk_f32 v245, v245, 0x437f0000, v196
	v_fmamk_f32 v246, v246, 0x437f0000, v196
	v_fmamk_f32 v247, v247, 0x437f0000, v196
	v_fmamk_f32 v248, v248, 0x437f0000, v196
	v_fmamk_f32 v249, v249, 0x437f0000, v196
	v_fmamk_f32 v250, v250, 0x437f0000, v196
	v_fmamk_f32 v251, v251, 0x437f0000, v196
	v_perm_b32 v236, v237, v236, s67
	v_perm_b32 v238, v239, v238, s67
	v_perm_b32 v240, v241, v240, s67
	v_perm_b32 v242, v243, v242, s67
	v_perm_b32 v244, v245, v244, s67
	v_perm_b32 v246, v247, v246, s67
	v_perm_b32 v248, v249, v248, s67
	v_perm_b32 v250, v251, v250, s67
	v_perm_b32 v4, v238, v236, s68
	v_perm_b32 v5, v242, v240, s68
	v_perm_b32 v6, v246, v244, s68
	v_perm_b32 v7, v250, v248, s68
	v_add_co_u32_e32 v8, vcc, s62, v2
	s_nop 1
	v_addc_co_u32_e32 v9, vcc, 0, v3, vcc
	global_store_dwordx4 v[8:9], v[4:7], off
	v_mul_f32_e32 v236, 0xbcb8aa3b, v94
	v_mul_f32_e32 v237, 0xbcb8aa3b, v95
	v_mul_f32_e32 v238, 0xbcb8aa3b, v96
	v_mul_f32_e32 v239, 0xbcb8aa3b, v97
	v_mul_f32_e32 v240, 0xbcb8aa3b, v90
	v_mul_f32_e32 v241, 0xbcb8aa3b, v91
	v_mul_f32_e32 v242, 0xbcb8aa3b, v92
	v_mul_f32_e32 v243, 0xbcb8aa3b, v93
	v_mul_f32_e32 v244, 0xbcb8aa3b, v86
	v_mul_f32_e32 v245, 0xbcb8aa3b, v87
	v_mul_f32_e32 v246, 0xbcb8aa3b, v88
	v_mul_f32_e32 v247, 0xbcb8aa3b, v89
	v_mul_f32_e32 v248, 0xbcb8aa3b, v82
	v_mul_f32_e32 v249, 0xbcb8aa3b, v83
	v_mul_f32_e32 v250, 0xbcb8aa3b, v84
	v_mul_f32_e32 v251, 0xbcb8aa3b, v85
	v_exp_f32_e32 v236, v236
	v_exp_f32_e32 v237, v237
	v_exp_f32_e32 v238, v238
	v_exp_f32_e32 v239, v239
	v_exp_f32_e32 v240, v240
	v_exp_f32_e32 v241, v241
	v_exp_f32_e32 v242, v242
	v_exp_f32_e32 v243, v243
	v_exp_f32_e32 v244, v244
	v_exp_f32_e32 v245, v245
	v_exp_f32_e32 v246, v246
	v_exp_f32_e32 v247, v247
	v_exp_f32_e32 v248, v248
	v_exp_f32_e32 v249, v249
	v_exp_f32_e32 v250, v250
	v_exp_f32_e32 v251, v251
	v_add_f32_e32 v236, 1.0, v236
	v_add_f32_e32 v237, 1.0, v237
	v_add_f32_e32 v238, 1.0, v238
	v_add_f32_e32 v239, 1.0, v239
	v_add_f32_e32 v240, 1.0, v240
	v_add_f32_e32 v241, 1.0, v241
	v_add_f32_e32 v242, 1.0, v242
	v_add_f32_e32 v243, 1.0, v243
	v_add_f32_e32 v244, 1.0, v244
	v_add_f32_e32 v245, 1.0, v245
	v_add_f32_e32 v246, 1.0, v246
	v_add_f32_e32 v247, 1.0, v247
	v_add_f32_e32 v248, 1.0, v248
	v_add_f32_e32 v249, 1.0, v249
	v_add_f32_e32 v250, 1.0, v250
	v_add_f32_e32 v251, 1.0, v251
	v_rcp_f32_e32 v236, v236
	v_rcp_f32_e32 v237, v237
	v_rcp_f32_e32 v238, v238
	v_rcp_f32_e32 v239, v239
	v_rcp_f32_e32 v240, v240
	v_rcp_f32_e32 v241, v241
	v_rcp_f32_e32 v242, v242
	v_rcp_f32_e32 v243, v243
	v_rcp_f32_e32 v244, v244
	v_rcp_f32_e32 v245, v245
	v_rcp_f32_e32 v246, v246
	v_rcp_f32_e32 v247, v247
	v_rcp_f32_e32 v248, v248
	v_rcp_f32_e32 v249, v249
	v_rcp_f32_e32 v250, v250
	v_rcp_f32_e32 v251, v251
	v_fmamk_f32 v236, v236, 0x437f0000, v196
	v_fmamk_f32 v237, v237, 0x437f0000, v196
	v_fmamk_f32 v238, v238, 0x437f0000, v196
	v_fmamk_f32 v239, v239, 0x437f0000, v196
	v_fmamk_f32 v240, v240, 0x437f0000, v196
	v_fmamk_f32 v241, v241, 0x437f0000, v196
	v_fmamk_f32 v242, v242, 0x437f0000, v196
	v_fmamk_f32 v243, v243, 0x437f0000, v196
	v_fmamk_f32 v244, v244, 0x437f0000, v196
	v_fmamk_f32 v245, v245, 0x437f0000, v196
	v_fmamk_f32 v246, v246, 0x437f0000, v196
	v_fmamk_f32 v247, v247, 0x437f0000, v196
	v_fmamk_f32 v248, v248, 0x437f0000, v196
	v_fmamk_f32 v249, v249, 0x437f0000, v196
	v_fmamk_f32 v250, v250, 0x437f0000, v196
	v_fmamk_f32 v251, v251, 0x437f0000, v196
	v_perm_b32 v236, v237, v236, s67
	v_perm_b32 v238, v239, v238, s67
	v_perm_b32 v240, v241, v240, s67
	v_perm_b32 v242, v243, v242, s67
	v_perm_b32 v244, v245, v244, s67
	v_perm_b32 v246, v247, v246, s67
	v_perm_b32 v248, v249, v248, s67
	v_perm_b32 v250, v251, v250, s67
	v_perm_b32 v4, v238, v236, s68
	v_perm_b32 v5, v242, v240, s68
	v_perm_b32 v6, v246, v244, s68
	v_perm_b32 v7, v250, v248, s68
	v_add_co_u32_e32 v8, vcc, s69, v2
	s_nop 1
	v_addc_co_u32_e32 v9, vcc, 0, v3, vcc
	global_store_dwordx4 v[8:9], v[4:7], off
	v_mul_f32_e32 v236, 0xbcb8aa3b, v78
	v_mul_f32_e32 v237, 0xbcb8aa3b, v79
	v_mul_f32_e32 v238, 0xbcb8aa3b, v80
	v_mul_f32_e32 v239, 0xbcb8aa3b, v81
	v_mul_f32_e32 v240, 0xbcb8aa3b, v74
	v_mul_f32_e32 v241, 0xbcb8aa3b, v75
	v_mul_f32_e32 v242, 0xbcb8aa3b, v76
	v_mul_f32_e32 v243, 0xbcb8aa3b, v77
	v_mul_f32_e32 v244, 0xbcb8aa3b, v70
	v_mul_f32_e32 v245, 0xbcb8aa3b, v71
	v_mul_f32_e32 v246, 0xbcb8aa3b, v72
	v_mul_f32_e32 v247, 0xbcb8aa3b, v73
	v_mul_f32_e32 v248, 0xbcb8aa3b, v66
	v_mul_f32_e32 v249, 0xbcb8aa3b, v67
	v_mul_f32_e32 v250, 0xbcb8aa3b, v68
	v_mul_f32_e32 v251, 0xbcb8aa3b, v69
	v_exp_f32_e32 v236, v236
	v_exp_f32_e32 v237, v237
	v_exp_f32_e32 v238, v238
	v_exp_f32_e32 v239, v239
	v_exp_f32_e32 v240, v240
	v_exp_f32_e32 v241, v241
	v_exp_f32_e32 v242, v242
	v_exp_f32_e32 v243, v243
	v_exp_f32_e32 v244, v244
	v_exp_f32_e32 v245, v245
	v_exp_f32_e32 v246, v246
	v_exp_f32_e32 v247, v247
; __device__ __forceinline__ float fsigmoid(float x) { return __builtin_amdgcn_rcpf(1.0f + __builtin_amdgcn_exp2f(-1.44269504f * x)); }
; __device__ __forceinline__ unsigned pk4_u8(float a, float b, float c, float d) {
;     const unsigned ya = __builtin_bit_cast(unsigned, a * 255.0f + 8388608.0f), yb = __builtin_bit_cast(unsigned, b * 255.0f + 8388608.0f), yc = __builtin_bit_cast(unsigned, c * 255.0f + 8388608.0f), yd = __builtin_bit_cast(unsigned, d * 255.0f + 8388608.0f);
;     const unsigned w01 = __builtin_amdgcn_perm(yb, ya, 0x0c0c0400u), w23 = __builtin_amdgcn_perm(yd, yc, 0x0c0c0400u);
;     return __builtin_amdgcn_perm(w23, w01, 0x05040100u); }
;     __device__ __forceinline__ void operator()(AccRef acc, const GUnit& u, int wr, int wc, int fr, int fq) const {
;         const int pm = u.x0, pn = u.x1; unsigned char* base = (pn < 8 ? GZF : GZS) + (size_t)(pm * 256 + wr * 64 + fr) * D + (pn & 7) * 256 + wc * 64 + 16 * fq;
; #pragma unroll
;         for (int ai = 0; ai < 2; ++ai)
; #pragma unroll
;             for (int m = 0; m < 4; ++m) { u32x4 w;
; #pragma unroll
;                 for (int bj = 0; bj < 2; ++bj)
; #pragma unroll
;                     for (int n = 0; n < 2; ++n) { const f32x4 v = acc[ai][bj][m][n]; w[bj * 2 + n] = pk4_u8(fsigmoid(v[0] * W8_INV), fsigmoid(v[1] * W8_INV), fsigmoid(v[2] * W8_INV), fsigmoid(v[3] * W8_INV)); }
;                 *(u32x4*)(base + (size_t)(ai * 128 + m * 16) * D) = w; }
	v_exp_f32_e32 v248, v248
	v_exp_f32_e32 v249, v249
	v_exp_f32_e32 v250, v250
	v_exp_f32_e32 v251, v251
	v_add_f32_e32 v236, 1.0, v236
	v_add_f32_e32 v237, 1.0, v237
	v_add_f32_e32 v238, 1.0, v238
	v_add_f32_e32 v239, 1.0, v239
	v_add_f32_e32 v240, 1.0, v240
	v_add_f32_e32 v241, 1.0, v241
	v_add_f32_e32 v242, 1.0, v242
	v_add_f32_e32 v243, 1.0, v243
	v_add_f32_e32 v244, 1.0, v244
	v_add_f32_e32 v245, 1.0, v245
	v_add_f32_e32 v246, 1.0, v246
	v_add_f32_e32 v247, 1.0, v247
	v_add_f32_e32 v248, 1.0, v248
	v_add_f32_e32 v249, 1.0, v249
	v_add_f32_e32 v250, 1.0, v250
	v_add_f32_e32 v251, 1.0, v251
	v_rcp_f32_e32 v236, v236
	v_rcp_f32_e32 v237, v237
	v_rcp_f32_e32 v238, v238
	v_rcp_f32_e32 v239, v239
	v_rcp_f32_e32 v240, v240
	v_rcp_f32_e32 v241, v241
	v_rcp_f32_e32 v242, v242
	v_rcp_f32_e32 v243, v243
	v_rcp_f32_e32 v244, v244
	v_rcp_f32_e32 v245, v245
	v_rcp_f32_e32 v246, v246
	v_rcp_f32_e32 v247, v247
	v_rcp_f32_e32 v248, v248
	v_rcp_f32_e32 v249, v249
	v_rcp_f32_e32 v250, v250
	v_rcp_f32_e32 v251, v251
	v_fmamk_f32 v236, v236, 0x437f0000, v196
	v_fmamk_f32 v237, v237, 0x437f0000, v196
	v_fmamk_f32 v238, v238, 0x437f0000, v196
	v_fmamk_f32 v239, v239, 0x437f0000, v196
	v_fmamk_f32 v240, v240, 0x437f0000, v196
	v_fmamk_f32 v241, v241, 0x437f0000, v196
	v_fmamk_f32 v242, v242, 0x437f0000, v196
	v_fmamk_f32 v243, v243, 0x437f0000, v196
	v_fmamk_f32 v244, v244, 0x437f0000, v196
	v_fmamk_f32 v245, v245, 0x437f0000, v196
	v_fmamk_f32 v246, v246, 0x437f0000, v196
	v_fmamk_f32 v247, v247, 0x437f0000, v196
	v_fmamk_f32 v248, v248, 0x437f0000, v196
	v_fmamk_f32 v249, v249, 0x437f0000, v196
	v_fmamk_f32 v250, v250, 0x437f0000, v196
	v_fmamk_f32 v251, v251, 0x437f0000, v196
	v_perm_b32 v236, v237, v236, s67
	v_perm_b32 v238, v239, v238, s67
	v_perm_b32 v240, v241, v240, s67
	v_perm_b32 v242, v243, v242, s67
	v_perm_b32 v244, v245, v244, s67
	v_perm_b32 v246, v247, v246, s67
	v_perm_b32 v248, v249, v248, s67
	v_perm_b32 v250, v251, v250, s67
	v_perm_b32 v4, v238, v236, s68
	v_perm_b32 v5, v242, v240, s68
	v_perm_b32 v6, v246, v244, s68
	v_perm_b32 v7, v250, v248, s68
	v_add_co_u32_e32 v8, vcc, s70, v2
	s_nop 1
	v_addc_co_u32_e32 v9, vcc, 0, v3, vcc
	global_store_dwordx4 v[8:9], v[4:7], off
	v_mul_f32_e32 v236, 0xbcb8aa3b, v62
	v_mul_f32_e32 v237, 0xbcb8aa3b, v63
	v_mul_f32_e32 v238, 0xbcb8aa3b, v64
	v_mul_f32_e32 v239, 0xbcb8aa3b, v65
	v_mul_f32_e32 v240, 0xbcb8aa3b, v58
	v_mul_f32_e32 v241, 0xbcb8aa3b, v59
	v_mul_f32_e32 v242, 0xbcb8aa3b, v60
	v_mul_f32_e32 v243, 0xbcb8aa3b, v61
	v_mul_f32_e32 v244, 0xbcb8aa3b, v54
	v_mul_f32_e32 v245, 0xbcb8aa3b, v55
	v_mul_f32_e32 v246, 0xbcb8aa3b, v56
	v_mul_f32_e32 v247, 0xbcb8aa3b, v57
	v_mul_f32_e32 v248, 0xbcb8aa3b, v50
	v_mul_f32_e32 v249, 0xbcb8aa3b, v51
	v_mul_f32_e32 v250, 0xbcb8aa3b, v52
	v_mul_f32_e32 v251, 0xbcb8aa3b, v53
	v_exp_f32_e32 v236, v236
	v_exp_f32_e32 v237, v237
	v_exp_f32_e32 v238, v238
	v_exp_f32_e32 v239, v239
	v_exp_f32_e32 v240, v240
	v_exp_f32_e32 v241, v241
	v_exp_f32_e32 v242, v242
	v_exp_f32_e32 v243, v243
	v_exp_f32_e32 v244, v244
	v_exp_f32_e32 v245, v245
	v_exp_f32_e32 v246, v246
	v_exp_f32_e32 v247, v247
	v_exp_f32_e32 v248, v248
	v_exp_f32_e32 v249, v249
	v_exp_f32_e32 v250, v250
	v_exp_f32_e32 v251, v251
	v_add_f32_e32 v236, 1.0, v236
	v_add_f32_e32 v237, 1.0, v237
	v_add_f32_e32 v238, 1.0, v238
	v_add_f32_e32 v239, 1.0, v239
	v_add_f32_e32 v240, 1.0, v240
	v_add_f32_e32 v241, 1.0, v241
	v_add_f32_e32 v242, 1.0, v242
	v_add_f32_e32 v243, 1.0, v243
	v_add_f32_e32 v244, 1.0, v244
	v_add_f32_e32 v245, 1.0, v245
	v_add_f32_e32 v246, 1.0, v246
	v_add_f32_e32 v247, 1.0, v247
	v_add_f32_e32 v248, 1.0, v248
	v_add_f32_e32 v249, 1.0, v249
	v_add_f32_e32 v250, 1.0, v250
	v_add_f32_e32 v251, 1.0, v251
	v_rcp_f32_e32 v236, v236
	v_rcp_f32_e32 v237, v237
	v_rcp_f32_e32 v238, v238
	v_rcp_f32_e32 v239, v239
	v_rcp_f32_e32 v240, v240
	v_rcp_f32_e32 v241, v241
	v_rcp_f32_e32 v242, v242
	v_rcp_f32_e32 v243, v243
	v_rcp_f32_e32 v244, v244
	v_rcp_f32_e32 v245, v245
	v_rcp_f32_e32 v246, v246
	v_rcp_f32_e32 v247, v247
	v_rcp_f32_e32 v248, v248
	v_rcp_f32_e32 v249, v249
	v_rcp_f32_e32 v250, v250
	v_rcp_f32_e32 v251, v251
	v_fmamk_f32 v236, v236, 0x437f0000, v196
	v_fmamk_f32 v237, v237, 0x437f0000, v196
	v_fmamk_f32 v238, v238, 0x437f0000, v196
	v_fmamk_f32 v239, v239, 0x437f0000, v196
; __device__ __forceinline__ float fsigmoid(float x) { return __builtin_amdgcn_rcpf(1.0f + __builtin_amdgcn_exp2f(-1.44269504f * x)); }
; #define PG8_BAR __builtin_amdgcn_s_barrier()
; template <class Epi, class Sched, bool ALIGN_EPI = true, bool F8 = false>
; __device__ __forceinline__ void gemm_phase(PG8_LAS unsigned char* lds, const Sched& S, const Epi& E) {
;     ...
;         E(acc, cur, wr, wc, fr, fq);
;         if (!has_next) break;
;         if (!(HasSeg<Epi>::v && cur.x2 == 0)) {
; #pragma unroll
;         for (int a = 0; a < 2; ++a)
; #pragma unroll
;             for (int b = 0; b < 2; ++b)
; #pragma unroll
;                 for (int m = 0; m < 4; ++m)
; #pragma unroll
;                     for (int n = 0; n < 2; ++n) acc[a][b][m][n] = (f32x4){0.f, 0.f, 0.f, 0.f};
;         }
;         cur = nxt; cA = nA; cB = nB; ++ui;
; #pragma unroll
;         for (int h = 0; h < 2; ++h)
; #pragma unroll
;             for (int i = 0; i < 2; ++i) voffA[h][i] = voffAn[h][i];
;         if constexpr (ALIGN_EPI) { if (wr == 1) PG8_BAR; }
;     }
;     __device__ __forceinline__ void operator()(AccRef acc, const GUnit& u, int wr, int wc, int fr, int fq) const {
;         const int pm = u.x0, pn = u.x1; unsigned char* base = (pn < 8 ? GZF : GZS) + (size_t)(pm * 256 + wr * 64 + fr) * D + (pn & 7) * 256 + wc * 64 + 16 * fq;
; #pragma unroll
;         for (int ai = 0; ai < 2; ++ai)
; #pragma unroll
;             for (int m = 0; m < 4; ++m) { u32x4 w;
; #pragma unroll
;                 for (int bj = 0; bj < 2; ++bj)
; #pragma unroll
;                     for (int n = 0; n < 2; ++n) { const f32x4 v = acc[ai][bj][m][n]; w[bj * 2 + n] = pk4_u8(fsigmoid(v[0] * W8_INV), fsigmoid(v[1] * W8_INV), fsigmoid(v[2] * W8_INV), fsigmoid(v[3] * W8_INV)); }
;                 *(u32x4*)(base + (size_t)(ai * 128 + m * 16) * D) = w; }
	v_fmamk_f32 v240, v240, 0x437f0000, v196
	v_fmamk_f32 v241, v241, 0x437f0000, v196
	v_fmamk_f32 v242, v242, 0x437f0000, v196
	v_fmamk_f32 v243, v243, 0x437f0000, v196
	v_fmamk_f32 v244, v244, 0x437f0000, v196
	v_fmamk_f32 v245, v245, 0x437f0000, v196
	v_fmamk_f32 v246, v246, 0x437f0000, v196
	v_fmamk_f32 v247, v247, 0x437f0000, v196
	v_fmamk_f32 v248, v248, 0x437f0000, v196
	v_fmamk_f32 v249, v249, 0x437f0000, v196
	v_fmamk_f32 v250, v250, 0x437f0000, v196
	v_fmamk_f32 v251, v251, 0x437f0000, v196
	v_perm_b32 v236, v237, v236, s67
	v_perm_b32 v238, v239, v238, s67
	v_perm_b32 v240, v241, v240, s67
	v_perm_b32 v242, v243, v242, s67
	v_perm_b32 v244, v245, v244, s67
	v_perm_b32 v246, v247, v246, s67
	v_perm_b32 v248, v249, v248, s67
	v_perm_b32 v250, v251, v250, s67
	v_perm_b32 v4, v238, v236, s68
	v_perm_b32 v5, v242, v240, s68
	v_perm_b32 v6, v246, v244, s68
	v_perm_b32 v7, v250, v248, s68
	v_add_co_u32_e32 v8, vcc, s71, v2
	s_nop 1
	v_addc_co_u32_e32 v9, vcc, 0, v3, vcc
	global_store_dwordx4 v[8:9], v[4:7], off
	v_mul_f32_e32 v236, 0xbcb8aa3b, v46
	v_mul_f32_e32 v237, 0xbcb8aa3b, v47
	v_mul_f32_e32 v238, 0xbcb8aa3b, v48
	v_mul_f32_e32 v239, 0xbcb8aa3b, v49
	v_mul_f32_e32 v240, 0xbcb8aa3b, v42
	v_mul_f32_e32 v241, 0xbcb8aa3b, v43
	v_mul_f32_e32 v242, 0xbcb8aa3b, v44
	v_mul_f32_e32 v243, 0xbcb8aa3b, v45
	v_mul_f32_e32 v244, 0xbcb8aa3b, v38
	v_mul_f32_e32 v245, 0xbcb8aa3b, v39
	v_mul_f32_e32 v246, 0xbcb8aa3b, v40
	v_mul_f32_e32 v247, 0xbcb8aa3b, v41
	v_mul_f32_e32 v248, 0xbcb8aa3b, v34
	v_mul_f32_e32 v249, 0xbcb8aa3b, v35
	v_mul_f32_e32 v250, 0xbcb8aa3b, v36
	v_mul_f32_e32 v251, 0xbcb8aa3b, v37
	v_exp_f32_e32 v236, v236
	v_exp_f32_e32 v237, v237
	v_exp_f32_e32 v238, v238
	v_exp_f32_e32 v239, v239
	v_exp_f32_e32 v240, v240
	v_exp_f32_e32 v241, v241
	v_exp_f32_e32 v242, v242
	v_exp_f32_e32 v243, v243
	v_exp_f32_e32 v244, v244
	v_exp_f32_e32 v245, v245
	v_exp_f32_e32 v246, v246
	v_exp_f32_e32 v247, v247
	v_exp_f32_e32 v248, v248
	v_exp_f32_e32 v249, v249
	v_exp_f32_e32 v250, v250
	v_exp_f32_e32 v251, v251
	v_add_f32_e32 v236, 1.0, v236
	v_add_f32_e32 v237, 1.0, v237
	v_add_f32_e32 v238, 1.0, v238
	v_add_f32_e32 v239, 1.0, v239
	v_add_f32_e32 v240, 1.0, v240
	v_add_f32_e32 v241, 1.0, v241
	v_add_f32_e32 v242, 1.0, v242
	v_add_f32_e32 v243, 1.0, v243
	v_add_f32_e32 v244, 1.0, v244
	v_add_f32_e32 v245, 1.0, v245
	v_add_f32_e32 v246, 1.0, v246
	v_add_f32_e32 v247, 1.0, v247
	v_add_f32_e32 v248, 1.0, v248
	v_add_f32_e32 v249, 1.0, v249
	v_add_f32_e32 v250, 1.0, v250
	v_add_f32_e32 v251, 1.0, v251
	v_rcp_f32_e32 v236, v236
	v_rcp_f32_e32 v237, v237
	v_rcp_f32_e32 v238, v238
	v_rcp_f32_e32 v239, v239
	v_rcp_f32_e32 v240, v240
	v_rcp_f32_e32 v241, v241
	v_rcp_f32_e32 v242, v242
	v_rcp_f32_e32 v243, v243
	v_rcp_f32_e32 v244, v244
	v_rcp_f32_e32 v245, v245
	v_rcp_f32_e32 v246, v246
	v_rcp_f32_e32 v247, v247
	v_rcp_f32_e32 v248, v248
	v_rcp_f32_e32 v249, v249
	v_rcp_f32_e32 v250, v250
	v_rcp_f32_e32 v251, v251
	v_fmamk_f32 v236, v236, 0x437f0000, v196
	v_fmamk_f32 v237, v237, 0x437f0000, v196
	v_fmamk_f32 v238, v238, 0x437f0000, v196
	v_fmamk_f32 v239, v239, 0x437f0000, v196
	v_fmamk_f32 v240, v240, 0x437f0000, v196
	v_fmamk_f32 v241, v241, 0x437f0000, v196
	v_fmamk_f32 v242, v242, 0x437f0000, v196
	v_fmamk_f32 v243, v243, 0x437f0000, v196
	v_fmamk_f32 v244, v244, 0x437f0000, v196
	v_fmamk_f32 v245, v245, 0x437f0000, v196
	v_fmamk_f32 v246, v246, 0x437f0000, v196
	v_fmamk_f32 v247, v247, 0x437f0000, v196
	v_fmamk_f32 v248, v248, 0x437f0000, v196
	v_fmamk_f32 v249, v249, 0x437f0000, v196
	v_fmamk_f32 v250, v250, 0x437f0000, v196
	v_fmamk_f32 v251, v251, 0x437f0000, v196
	v_perm_b32 v236, v237, v236, s67
	v_perm_b32 v238, v239, v238, s67
	v_perm_b32 v240, v241, v240, s67
	v_perm_b32 v242, v243, v242, s67
	v_perm_b32 v244, v245, v244, s67
	v_perm_b32 v246, v247, v246, s67
	v_perm_b32 v248, v249, v248, s67
	v_perm_b32 v250, v251, v250, s67
	v_perm_b32 v4, v238, v236, s68
	v_perm_b32 v5, v242, v240, s68
	v_perm_b32 v6, v246, v244, s68
	v_perm_b32 v7, v250, v248, s68
	v_add_co_u32_e32 v8, vcc, 0x58000, v2
	s_nop 1
	v_addc_co_u32_e32 v9, vcc, 0, v3, vcc
	global_store_dwordx4 v[8:9], v[4:7], off
	s_andn2_b64 vcc, exec, s[0:1]
	s_mov_b64 s[0:1], -1
	s_cbranch_vccnz .LBB0_420
	s_andn2_b64 vcc, exec, s[10:11]
	s_cbranch_vccnz .LBB0_419
	s_branch .LBB0_419
